# LDS-DMA staging of 16 Wv fragments + loop-edge fall-through layout + exact vmcnt on the last three tiles
# speedup vs baseline: 1.0009x; 1.0009x over previous
.Lring_w0_2:
	s_waitcnt vmcnt(18)
	s_branch .Lring_go_2
.Lring_w0_3:
	s_waitcnt vmcnt(9)
	s_branch .Lring_go_3
